# v043 + grid barrier: census words read back to back, arrival ticket issued without waiting for them, first-barrier census branch bypassed inside the layer loop
# baseline (speedup 1.0000x reference)
; __device__ __forceinline__ unsigned xb_add(unsigned* p, unsigned v) { return __hip_atomic_fetch_add(p, v, __ATOMIC_RELAXED, __HIP_MEMORY_SCOPE_AGENT); }
; __device__ __forceinline__ void xcd_barrier(const XcdBarrier& b) {
;     asm volatile("s_waitcnt vmcnt(0)" ::: "memory");
;     __syncthreads();
;     if (threadIdx.x == 0) {
;         unsigned* bar = b.bar;
;         __builtin_amdgcn_s_waitcnt(0);
;         unsigned nloc = b.st[0], nx = b.st[1];
;         if (nloc == 0u) { xcd_barrier_complete(bar, b.x, nloc, nx); b.st[0] = nloc; b.st[1] = nx; }
;         const unsigned old = xb_add(&bar[XB_XSUB(b.x)], 1u);
.LBB0_283:
	s_waitcnt vmcnt(0)
	s_waitcnt vmcnt(0) lgkmcnt(0)
	s_barrier
	s_mov_b64 s[0:1], exec
	v_readlane_b32 s6, v253, 2
	v_readlane_b32 s7, v253, 3
	s_and_b64 s[6:7], s[0:1], s[6:7]
	s_mov_b64 exec, s[6:7]
	s_cbranch_execz .LBB0_335
	v_readlane_b32 s5, v255, 15
	s_waitcnt vmcnt(0) expcnt(0) lgkmcnt(0)
	s_nop 0
	v_mov_b32_e32 v1, s5
	ds_read_b32 v3, v1
	v_readlane_b32 s5, v255, 16
	s_nop 1
	v_mov_b32_e32 v1, s5
	ds_read_b32 v2, v1
	s_branch .LBB0_299
	v_readlane_b32 s8, v253, 0
	v_readlane_b32 s9, v253, 1
	s_load_dwordx2 s[6:7], s[8:9], 0x4
	s_mov_b32 s11, 1
	s_waitcnt lgkmcnt(0)
	s_mul_i32 s5, s6, s68
	s_mul_i32 s5, s5, s7
	s_branch .LBB0_287

; __device__ __forceinline__ unsigned xb_add(unsigned* p, unsigned v) { return __hip_atomic_fetch_add(p, v, __ATOMIC_RELAXED, __HIP_MEMORY_SCOPE_AGENT); }
; __device__ __forceinline__ void xcd_barrier(const XcdBarrier& b) {
;     asm volatile("s_waitcnt vmcnt(0)" ::: "memory");
;     __syncthreads();
;     if (threadIdx.x == 0) {
;         unsigned* bar = b.bar;
;         __builtin_amdgcn_s_waitcnt(0);
;         unsigned nloc = b.st[0], nx = b.st[1];
;         if (nloc == 0u) { xcd_barrier_complete(bar, b.x, nloc, nx); b.st[0] = nloc; b.st[1] = nx; }
;         const unsigned old = xb_add(&bar[XB_XSUB(b.x)], 1u);
.LBB0_359:
	s_add_i32 s4, s87, 4
	s_cmp_ge_i32 s4, s57
	s_cbranch_scc1 .LBB0_413
	s_waitcnt vmcnt(0)
	s_waitcnt vmcnt(0)
	s_barrier
	s_mov_b64 s[0:1], exec
	v_readlane_b32 s6, v253, 2
	v_readlane_b32 s7, v253, 3
	s_and_b64 s[6:7], s[0:1], s[6:7]
	s_mov_b64 exec, s[6:7]
	s_cbranch_execz .LBB0_412
	v_readlane_b32 s5, v255, 15
	s_waitcnt vmcnt(0) expcnt(0) lgkmcnt(0)
	s_nop 0
	v_mov_b32_e32 v1, s5
	ds_read_b32 v3, v1
	v_readlane_b32 s5, v255, 16
	s_nop 1
	v_mov_b32_e32 v1, s5
	ds_read_b32 v2, v1
	s_branch .LBB0_376
	v_readlane_b32 s8, v253, 0
	v_readlane_b32 s9, v253, 1
	s_load_dwordx2 s[6:7], s[8:9], 0x4
	s_mov_b32 s11, 1
	s_waitcnt lgkmcnt(0)
	s_mul_i32 s5, s6, s68
	s_mul_i32 s5, s5, s7
	s_branch .LBB0_364

; __device__ __forceinline__ unsigned xb_add(unsigned* p, unsigned v) { return __hip_atomic_fetch_add(p, v, __ATOMIC_RELAXED, __HIP_MEMORY_SCOPE_AGENT); }
; __device__ __forceinline__ void xcd_barrier(const XcdBarrier& b) {
;     asm volatile("s_waitcnt vmcnt(0)" ::: "memory");
;     __syncthreads();
;     if (threadIdx.x == 0) {
;         unsigned* bar = b.bar;
;         __builtin_amdgcn_s_waitcnt(0);
;         unsigned nloc = b.st[0], nx = b.st[1];
;         if (nloc == 0u) { xcd_barrier_complete(bar, b.x, nloc, nx); b.st[0] = nloc; b.st[1] = nx; }
;         const unsigned old = xb_add(&bar[XB_XSUB(b.x)], 1u);
.LBB0_474:
	s_add_i32 s4, s87, 5
	s_cmp_ge_i32 s4, s57
	s_cbranch_scc1 .LBB0_528
	s_waitcnt vmcnt(0)
	s_waitcnt vmcnt(0) lgkmcnt(0)
	s_barrier
	s_mov_b64 s[0:1], exec
	v_readlane_b32 s6, v253, 2
	v_readlane_b32 s7, v253, 3
	s_and_b64 s[6:7], s[0:1], s[6:7]
	s_mov_b64 exec, s[6:7]
	s_cbranch_execz .LBB0_527
	v_readlane_b32 s5, v255, 15
	s_waitcnt vmcnt(0) expcnt(0) lgkmcnt(0)
	s_nop 0
	v_mov_b32_e32 v1, s5
	ds_read_b32 v3, v1
	v_readlane_b32 s5, v255, 16
	s_nop 1
	v_mov_b32_e32 v1, s5
	ds_read_b32 v2, v1
	s_branch .LBB0_491
	v_readlane_b32 s8, v253, 0
	v_readlane_b32 s9, v253, 1
	s_load_dwordx2 s[6:7], s[8:9], 0x4
	s_mov_b32 s11, 1
	s_waitcnt lgkmcnt(0)
	s_mul_i32 s5, s6, s68
	s_mul_i32 s5, s5, s7
	s_branch .LBB0_479

; __device__ __forceinline__ unsigned xb_add(unsigned* p, unsigned v) { return __hip_atomic_fetch_add(p, v, __ATOMIC_RELAXED, __HIP_MEMORY_SCOPE_AGENT); }
; __device__ __forceinline__ void xcd_barrier(const XcdBarrier& b) {
;     asm volatile("s_waitcnt vmcnt(0)" ::: "memory");
;     __syncthreads();
;     if (threadIdx.x == 0) {
;         unsigned* bar = b.bar;
;         __builtin_amdgcn_s_waitcnt(0);
;         unsigned nloc = b.st[0], nx = b.st[1];
;         if (nloc == 0u) { xcd_barrier_complete(bar, b.x, nloc, nx); b.st[0] = nloc; b.st[1] = nx; }
;         const unsigned old = xb_add(&bar[XB_XSUB(b.x)], 1u);
.LBB0_703:
	s_or_b64 exec, exec, s[6:7]
	s_add_i32 s4, s87, 6
	v_readlane_b32 s76, v253, 4
	s_cmp_ge_i32 s4, s57
	v_readlane_b32 s77, v253, 5
	v_readlane_b32 s36, v255, 56
	v_readlane_b32 s52, v255, 57
	v_readlane_b32 s71, v255, 58
	s_movk_i32 s75, 0x100
	s_mov_b32 s25, 0x38600000
	s_cbranch_scc1 .LBB0_757
	s_waitcnt vmcnt(0)
	s_waitcnt lgkmcnt(0)
	s_barrier
	s_mov_b64 s[0:1], exec
	v_readlane_b32 s6, v253, 2
	v_readlane_b32 s7, v253, 3
	s_and_b64 s[6:7], s[0:1], s[6:7]
	s_mov_b64 exec, s[6:7]
	s_cbranch_execz .LBB0_756
	v_readlane_b32 s5, v255, 15
	s_waitcnt vmcnt(0) expcnt(0) lgkmcnt(0)
	s_nop 0
	v_mov_b32_e32 v1, s5
	ds_read_b32 v3, v1
	v_readlane_b32 s5, v255, 16
	s_nop 1
	v_mov_b32_e32 v1, s5
	ds_read_b32 v2, v1
	s_branch .LBB0_720
	v_readlane_b32 s8, v253, 0
	v_readlane_b32 s9, v253, 1
	s_load_dwordx2 s[6:7], s[8:9], 0x4
	s_mov_b32 s11, 1
	s_waitcnt lgkmcnt(0)
	s_mul_i32 s5, s6, s68
	s_mul_i32 s5, s5, s7
	s_branch .LBB0_708

; __device__ __forceinline__ unsigned xb_add(unsigned* p, unsigned v) { return __hip_atomic_fetch_add(p, v, __ATOMIC_RELAXED, __HIP_MEMORY_SCOPE_AGENT); }
; __device__ __forceinline__ void xcd_barrier(const XcdBarrier& b) {
;     asm volatile("s_waitcnt vmcnt(0)" ::: "memory");
;     __syncthreads();
;     if (threadIdx.x == 0) {
;         unsigned* bar = b.bar;
;         __builtin_amdgcn_s_waitcnt(0);
;         unsigned nloc = b.st[0], nx = b.st[1];
;         if (nloc == 0u) { xcd_barrier_complete(bar, b.x, nloc, nx); b.st[0] = nloc; b.st[1] = nx; }
;         const unsigned old = xb_add(&bar[XB_XSUB(b.x)], 1u);
.LBB0_800:
	s_add_i32 s4, s87, 7
	s_cmp_lt_i32 s4, s57
	s_cbranch_scc0 .LBB0_854
	s_waitcnt vmcnt(0)
	s_waitcnt vmcnt(0) lgkmcnt(0)
	s_barrier
	s_mov_b64 s[0:1], exec
	v_readlane_b32 s6, v253, 2
	v_readlane_b32 s7, v253, 3
	s_and_b64 s[6:7], s[0:1], s[6:7]
	s_mov_b64 exec, s[6:7]
	s_cbranch_execz .LBB0_853
	v_readlane_b32 s5, v255, 15
	s_waitcnt vmcnt(0) expcnt(0) lgkmcnt(0)
	s_nop 0
	v_mov_b32_e32 v1, s5
	ds_read_b32 v3, v1
	v_readlane_b32 s5, v255, 16
	s_nop 1
	v_mov_b32_e32 v1, s5
	ds_read_b32 v2, v1
	s_branch .LBB0_817
	v_readlane_b32 s8, v253, 0
	v_readlane_b32 s9, v253, 1
	s_load_dwordx2 s[6:7], s[8:9], 0x4
	s_mov_b32 s11, 1
	s_waitcnt lgkmcnt(0)
	s_mul_i32 s5, s6, s68
	s_mul_i32 s5, s5, s7
	s_branch .LBB0_805

; __device__ __forceinline__ unsigned xb_add(unsigned* p, unsigned v) { return __hip_atomic_fetch_add(p, v, __ATOMIC_RELAXED, __HIP_MEMORY_SCOPE_AGENT); }
; __device__ __forceinline__ void xcd_barrier(const XcdBarrier& b) {
;     asm volatile("s_waitcnt vmcnt(0)" ::: "memory");
;     __syncthreads();
;     if (threadIdx.x == 0) {
;         unsigned* bar = b.bar;
;         __builtin_amdgcn_s_waitcnt(0);
;         unsigned nloc = b.st[0], nx = b.st[1];
;         if (nloc == 0u) { xcd_barrier_complete(bar, b.x, nloc, nx); b.st[0] = nloc; b.st[1] = nx; }
;         const unsigned old = xb_add(&bar[XB_XSUB(b.x)], 1u);
.LBB0_925:
	v_readlane_b32 s87, v255, 59
	s_add_i32 s4, s87, 8
	s_cmp_ge_i32 s4, s57
	s_cbranch_scc1 .LBB0_937
	s_waitcnt vmcnt(0)
	s_waitcnt vmcnt(0)
	s_barrier
	s_mov_b64 s[0:1], exec
	v_readlane_b32 s6, v253, 2
	v_readlane_b32 s7, v253, 3
	s_and_b64 s[6:7], s[0:1], s[6:7]
	s_mov_b32 s85, 0x10000
	s_mov_b64 exec, s[6:7]
	s_cbranch_execz .LBB0_979
	v_readlane_b32 s5, v255, 15
	s_waitcnt vmcnt(0) expcnt(0) lgkmcnt(0)
	s_nop 0
	v_mov_b32_e32 v1, s5
	ds_read_b32 v3, v1
	v_readlane_b32 s5, v255, 16
	s_nop 1
	v_mov_b32_e32 v1, s5
	ds_read_b32 v2, v1
	s_branch .LBB0_943
	v_readlane_b32 s8, v253, 0
	v_readlane_b32 s9, v253, 1
	s_load_dwordx2 s[6:7], s[8:9], 0x4
	s_mov_b32 s11, 1
	s_waitcnt lgkmcnt(0)
	s_mul_i32 s5, s6, s68
	s_mul_i32 s5, s5, s7
	s_branch .LBB0_930

; __device__ __forceinline__ unsigned xb_add(unsigned* p, unsigned v) { return __hip_atomic_fetch_add(p, v, __ATOMIC_RELAXED, __HIP_MEMORY_SCOPE_AGENT); }
; __device__ __forceinline__ void xcd_barrier(const XcdBarrier& b) {
;     asm volatile("s_waitcnt vmcnt(0)" ::: "memory");
;     __syncthreads();
;     if (threadIdx.x == 0) {
;         unsigned* bar = b.bar;
;         __builtin_amdgcn_s_waitcnt(0);
;         unsigned nloc = b.st[0], nx = b.st[1];
;         if (nloc == 0u) { xcd_barrier_complete(bar, b.x, nloc, nx); b.st[0] = nloc; b.st[1] = nx; }
;         const unsigned old = xb_add(&bar[XB_XSUB(b.x)], 1u);
.LBB0_986:
	s_movk_i32 s10, 0x3fff
	s_or_b64 exec, exec, s[0:1]
	s_add_i32 s4, s87, 9
	s_cmp_ge_i32 s4, s57
	s_cbranch_scc1 .LBB0_1040
	s_waitcnt vmcnt(0)
	s_waitcnt vmcnt(0)
	s_barrier
	s_mov_b64 s[0:1], exec
	v_readlane_b32 s6, v253, 2
	v_readlane_b32 s7, v253, 3
	s_and_b64 s[6:7], s[0:1], s[6:7]
	s_mov_b64 exec, s[6:7]
	s_cbranch_execz .LBB0_1039
	v_readlane_b32 s5, v255, 15
	s_waitcnt vmcnt(0) expcnt(0) lgkmcnt(0)
	s_nop 0
	v_mov_b32_e32 v1, s5
	ds_read_b32 v3, v1
	v_readlane_b32 s5, v255, 16
	s_nop 1
	v_mov_b32_e32 v1, s5
	ds_read_b32 v2, v1
	s_branch .LBB0_1003
	v_readlane_b32 s8, v253, 0
	v_readlane_b32 s9, v253, 1
	s_load_dwordx2 s[6:7], s[8:9], 0x4
	s_mov_b32 s11, 1
	s_waitcnt lgkmcnt(0)
	s_mul_i32 s5, s6, s68
	s_mul_i32 s5, s5, s7
	s_branch .LBB0_991

; __device__ __forceinline__ unsigned xb_add(unsigned* p, unsigned v) { return __hip_atomic_fetch_add(p, v, __ATOMIC_RELAXED, __HIP_MEMORY_SCOPE_AGENT); }
; __device__ __forceinline__ void xcd_barrier(const XcdBarrier& b) {
;     asm volatile("s_waitcnt vmcnt(0)" ::: "memory");
;     __syncthreads();
;     if (threadIdx.x == 0) {
;         unsigned* bar = b.bar;
;         __builtin_amdgcn_s_waitcnt(0);
;         unsigned nloc = b.st[0], nx = b.st[1];
;         if (nloc == 0u) { xcd_barrier_complete(bar, b.x, nloc, nx); b.st[0] = nloc; b.st[1] = nx; }
;         const unsigned old = xb_add(&bar[XB_XSUB(b.x)], 1u);
.LBB0_1063:
	s_add_i32 s4, s87, 10
	s_cmp_ge_i32 s4, s57
	s_cbranch_scc1 .LBB0_1117
	s_waitcnt vmcnt(0)
	s_waitcnt vmcnt(0)
	s_barrier
	s_mov_b64 s[0:1], exec
	v_readlane_b32 s6, v253, 2
	v_readlane_b32 s7, v253, 3
	s_and_b64 s[6:7], s[0:1], s[6:7]
	s_mov_b64 exec, s[6:7]
	s_cbranch_execz .LBB0_1116
	v_readlane_b32 s5, v255, 15
	s_waitcnt vmcnt(0) expcnt(0) lgkmcnt(0)
	s_nop 0
	v_mov_b32_e32 v1, s5
	ds_read_b32 v3, v1
	v_readlane_b32 s5, v255, 16
	s_nop 1
	v_mov_b32_e32 v1, s5
	ds_read_b32 v2, v1
	s_branch .LBB0_1080
	v_readlane_b32 s8, v253, 0
	v_readlane_b32 s9, v253, 1
	s_load_dwordx2 s[6:7], s[8:9], 0x4
	s_mov_b32 s11, 1
	s_waitcnt lgkmcnt(0)
	s_mul_i32 s5, s6, s68
	s_mul_i32 s5, s5, s7
	s_branch .LBB0_1068

; __device__ __forceinline__ unsigned xb_add(unsigned* p, unsigned v) { return __hip_atomic_fetch_add(p, v, __ATOMIC_RELAXED, __HIP_MEMORY_SCOPE_AGENT); }
; __device__ __forceinline__ void xcd_barrier(const XcdBarrier& b) {
;     asm volatile("s_waitcnt vmcnt(0)" ::: "memory");
;     __syncthreads();
;     if (threadIdx.x == 0) {
;         unsigned* bar = b.bar;
;         __builtin_amdgcn_s_waitcnt(0);
;         unsigned nloc = b.st[0], nx = b.st[1];
;         if (nloc == 0u) { xcd_barrier_complete(bar, b.x, nloc, nx); b.st[0] = nloc; b.st[1] = nx; }
;         const unsigned old = xb_add(&bar[XB_XSUB(b.x)], 1u);
.LBB0_1139:
	s_add_i32 s4, s87, 11
	s_cmp_ge_i32 s4, s57
	s_cbranch_scc1 .LBB0_1193
	s_waitcnt vmcnt(0)
	s_waitcnt vmcnt(0)
	s_barrier
	s_mov_b64 s[0:1], exec
	v_readlane_b32 s6, v253, 2
	v_readlane_b32 s7, v253, 3
	s_and_b64 s[6:7], s[0:1], s[6:7]
	s_mov_b64 exec, s[6:7]
	s_cbranch_execz .LBB0_1192
	v_readlane_b32 s5, v255, 15
	s_waitcnt vmcnt(0) expcnt(0) lgkmcnt(0)
	s_nop 0
	v_mov_b32_e32 v1, s5
	ds_read_b32 v3, v1
	v_readlane_b32 s5, v255, 16
	s_nop 1
	v_mov_b32_e32 v1, s5
	ds_read_b32 v2, v1
	s_branch .LBB0_1156
	v_readlane_b32 s8, v253, 0
	v_readlane_b32 s9, v253, 1
	s_load_dwordx2 s[6:7], s[8:9], 0x4
	s_mov_b32 s11, 1
	s_waitcnt lgkmcnt(0)
	s_mul_i32 s5, s6, s68
	s_mul_i32 s5, s5, s7
	s_branch .LBB0_1144

; __device__ __forceinline__ unsigned xb_add(unsigned* p, unsigned v) { return __hip_atomic_fetch_add(p, v, __ATOMIC_RELAXED, __HIP_MEMORY_SCOPE_AGENT); }
; __device__ __forceinline__ void xcd_barrier(const XcdBarrier& b) {
;     asm volatile("s_waitcnt vmcnt(0)" ::: "memory");
;     __syncthreads();
;     if (threadIdx.x == 0) {
;         unsigned* bar = b.bar;
;         __builtin_amdgcn_s_waitcnt(0);
;         unsigned nloc = b.st[0], nx = b.st[1];
;         if (nloc == 0u) { xcd_barrier_complete(bar, b.x, nloc, nx); b.st[0] = nloc; b.st[1] = nx; }
;         const unsigned old = xb_add(&bar[XB_XSUB(b.x)], 1u);
.LBB0_1260:
	s_add_i32 s4, s87, 12
	s_cmp_ge_i32 s4, s57
	s_cbranch_scc1 .LBB0_1272
	s_waitcnt vmcnt(0)
	s_waitcnt vmcnt(0)
	s_barrier
	s_mov_b64 s[0:1], exec
	v_readlane_b32 s6, v253, 2
	v_readlane_b32 s7, v253, 3
	s_and_b64 s[6:7], s[0:1], s[6:7]
	s_movk_i32 s62, 0x2000
	s_mov_b64 exec, s[6:7]
	s_cbranch_execz .LBB0_1314
	v_readlane_b32 s5, v255, 15
	s_waitcnt vmcnt(0) expcnt(0) lgkmcnt(0)
	s_nop 0
	v_mov_b32_e32 v1, s5
	ds_read_b32 v3, v1
	v_readlane_b32 s5, v255, 16
	s_nop 1
	v_mov_b32_e32 v1, s5
	ds_read_b32 v2, v1
	s_branch .LBB0_1278
	v_readlane_b32 s8, v253, 0
	v_readlane_b32 s9, v253, 1
	s_load_dwordx2 s[6:7], s[8:9], 0x4
	s_mov_b32 s11, 1
	s_waitcnt lgkmcnt(0)
	s_mul_i32 s5, s6, s68
	s_mul_i32 s5, s5, s7
	s_branch .LBB0_1265

; __device__ __forceinline__ unsigned xb_add(unsigned* p, unsigned v) { return __hip_atomic_fetch_add(p, v, __ATOMIC_RELAXED, __HIP_MEMORY_SCOPE_AGENT); }
; __device__ __forceinline__ void xcd_barrier(const XcdBarrier& b) {
;     asm volatile("s_waitcnt vmcnt(0)" ::: "memory");
;     __syncthreads();
;     if (threadIdx.x == 0) {
;         unsigned* bar = b.bar;
;         __builtin_amdgcn_s_waitcnt(0);
;         unsigned nloc = b.st[0], nx = b.st[1];
;         if (nloc == 0u) { xcd_barrier_complete(bar, b.x, nloc, nx); b.st[0] = nloc; b.st[1] = nx; }
;         const unsigned old = xb_add(&bar[XB_XSUB(b.x)], 1u);
.LBB0_1382:
	s_add_i32 s4, s87, 13
	s_cmp_ge_i32 s4, s57
	s_cbranch_scc1 .LBB0_1436
	s_waitcnt vmcnt(0)
	s_waitcnt vmcnt(0) lgkmcnt(0)
	s_barrier
	s_mov_b64 s[0:1], exec
	v_readlane_b32 s6, v253, 2
	v_readlane_b32 s7, v253, 3
	s_and_b64 s[6:7], s[0:1], s[6:7]
	s_mov_b64 exec, s[6:7]
	s_cbranch_execz .LBB0_1435
	v_readlane_b32 s5, v255, 15
	s_waitcnt vmcnt(0) expcnt(0) lgkmcnt(0)
	s_nop 0
	v_mov_b32_e32 v1, s5
	ds_read_b32 v3, v1
	v_readlane_b32 s5, v255, 16
	s_nop 1
	v_mov_b32_e32 v1, s5
	ds_read_b32 v2, v1
	s_branch .LBB0_1399
	v_readlane_b32 s8, v253, 0
	v_readlane_b32 s9, v253, 1
	s_load_dwordx2 s[6:7], s[8:9], 0x4
	s_mov_b32 s11, 1
	s_waitcnt lgkmcnt(0)
	s_mul_i32 s5, s6, s68
	s_mul_i32 s5, s5, s7
	s_branch .LBB0_1387

; __device__ __forceinline__ unsigned xb_add(unsigned* p, unsigned v) { return __hip_atomic_fetch_add(p, v, __ATOMIC_RELAXED, __HIP_MEMORY_SCOPE_AGENT); }
; __device__ __forceinline__ void xcd_barrier(const XcdBarrier& b) {
;     asm volatile("s_waitcnt vmcnt(0)" ::: "memory");
;     __syncthreads();
;     if (threadIdx.x == 0) {
;         unsigned* bar = b.bar;
;         __builtin_amdgcn_s_waitcnt(0);
;         unsigned nloc = b.st[0], nx = b.st[1];
;         if (nloc == 0u) { xcd_barrier_complete(bar, b.x, nloc, nx); b.st[0] = nloc; b.st[1] = nx; }
;         const unsigned old = xb_add(&bar[XB_XSUB(b.x)], 1u);
.LBB0_1444:
	s_or_b64 exec, exec, s[0:1]
	s_add_i32 s4, s87, 14
	s_cmp_ge_i32 s4, s57
	s_cbranch_scc1 .LBB0_1498
	s_waitcnt vmcnt(0)
	s_waitcnt vmcnt(0)
	s_barrier
	s_mov_b64 s[0:1], exec
	v_readlane_b32 s6, v253, 2
	v_readlane_b32 s7, v253, 3
	s_and_b64 s[6:7], s[0:1], s[6:7]
	s_mov_b64 exec, s[6:7]
	s_cbranch_execz .LBB0_1497
	v_readlane_b32 s5, v255, 15
	s_waitcnt vmcnt(0) expcnt(0) lgkmcnt(0)
	s_nop 0
	v_mov_b32_e32 v1, s5
	ds_read_b32 v3, v1
	v_readlane_b32 s5, v255, 16
	s_nop 1
	v_mov_b32_e32 v1, s5
	ds_read_b32 v2, v1
	s_branch .LBB0_1461
	v_readlane_b32 s8, v253, 0
	v_readlane_b32 s9, v253, 1
	s_load_dwordx2 s[6:7], s[8:9], 0x4
	s_mov_b32 s11, 1
	s_waitcnt lgkmcnt(0)
	s_mul_i32 s5, s6, s68
	s_mul_i32 s5, s5, s7
	s_branch .LBB0_1449
